# v39 + GEMM2: in-place fp8 pack of both accumulator halves (ai=0 under the 4th-phase MFMAs; ai=1 by the early wave half while it waits, by the late half right after its MFMAs); no pack arithmetic left
# baseline (speedup 1.0000x reference)
; #define PG8_BAR __builtin_amdgcn_s_barrier()
;     ...
;         if constexpr (ALIGN_EPI) { if (wr == 0) PG8_BAR; }
;         if constexpr (Epi::F8) asm volatile("s_nop 15\n\ts_nop 15" ::: "memory");
;         if (!(probe & 2)) E(acc, cur, wr, wc, fr, fq);
;     __device__ __forceinline__ u32x4 pack(const f32x4 (&acc)[2][2][4][2], int ai, int m) const {
;         u32x4 w;
; #pragma unroll
;         for (int bj = 0; bj < 2; ++bj) {
;             f32x4 v0 = acc[ai][bj][m][0], v1 = acc[ai][bj][m][1];
; #pragma unroll
;             for (int j = 0; j < 4; ++j) { v0[j] = fminf(fmaxf(v0[j], -448.f), 448.f); v1[j] = fminf(fmaxf(v1[j], -448.f), 448.f); }
;             int w0 = __builtin_amdgcn_cvt_pk_fp8_f32(v0[0], v0[1], 0, false); w0 = __builtin_amdgcn_cvt_pk_fp8_f32(v0[2], v0[3], w0, true);
;             int w1 = __builtin_amdgcn_cvt_pk_fp8_f32(v1[0], v1[1], 0, false); w1 = __builtin_amdgcn_cvt_pk_fp8_f32(v1[2], v1[3], w1, true);
;             if (bj == 0) { w.x = (unsigned)w0; w.y = (unsigned)w1; } else { w.z = (unsigned)w0; w.w = (unsigned)w1; } }
;         return w;
;     }
.LBB0_843:
	s_barrier
	s_andn2_b64 vcc, exec, s[52:53]
	s_cbranch_vccnz .Lg2q_w1_0
	s_nop 15
	s_nop 3
	v_med3_f32 v128, v128, s29, v227
	v_med3_f32 v129, v129, s29, v227
	v_med3_f32 v130, v130, s29, v227
	v_med3_f32 v131, v131, s29, v227
	v_cvt_pk_fp8_f32 v128, v128, v129
	v_cvt_pk_fp8_f32 v128, v130, v131 op_sel:[0,0,1]
	v_med3_f32 v124, v124, s29, v227
	v_med3_f32 v125, v125, s29, v227
	v_med3_f32 v126, v126, s29, v227
	v_med3_f32 v127, v127, s29, v227
	v_cvt_pk_fp8_f32 v129, v124, v125
	v_cvt_pk_fp8_f32 v129, v126, v127 op_sel:[0,0,1]
	v_med3_f32 v160, v160, s29, v227
	v_med3_f32 v161, v161, s29, v227
	v_med3_f32 v162, v162, s29, v227
	v_med3_f32 v163, v163, s29, v227
	v_cvt_pk_fp8_f32 v130, v160, v161
	v_cvt_pk_fp8_f32 v130, v162, v163 op_sel:[0,0,1]
	v_med3_f32 v156, v156, s29, v227
	v_med3_f32 v157, v157, s29, v227
	v_med3_f32 v158, v158, s29, v227
	v_med3_f32 v159, v159, s29, v227
	v_cvt_pk_fp8_f32 v131, v156, v157
	v_cvt_pk_fp8_f32 v131, v158, v159 op_sel:[0,0,1]
	v_med3_f32 v108, v108, s29, v227
	v_med3_f32 v109, v109, s29, v227
	v_med3_f32 v110, v110, s29, v227
	v_med3_f32 v111, v111, s29, v227
	v_cvt_pk_fp8_f32 v108, v108, v109
	v_cvt_pk_fp8_f32 v108, v110, v111 op_sel:[0,0,1]
	v_med3_f32 v104, v104, s29, v227
	v_med3_f32 v105, v105, s29, v227
	v_med3_f32 v106, v106, s29, v227
	v_med3_f32 v107, v107, s29, v227
	v_cvt_pk_fp8_f32 v109, v104, v105
	v_cvt_pk_fp8_f32 v109, v106, v107 op_sel:[0,0,1]
	v_med3_f32 v140, v140, s29, v227
	v_med3_f32 v141, v141, s29, v227
	v_med3_f32 v142, v142, s29, v227
	v_med3_f32 v143, v143, s29, v227
	v_cvt_pk_fp8_f32 v110, v140, v141
	v_cvt_pk_fp8_f32 v110, v142, v143 op_sel:[0,0,1]
	v_med3_f32 v132, v132, s29, v227
	v_med3_f32 v133, v133, s29, v227
	v_med3_f32 v134, v134, s29, v227
	v_med3_f32 v135, v135, s29, v227
	v_cvt_pk_fp8_f32 v111, v132, v133
	v_cvt_pk_fp8_f32 v111, v134, v135 op_sel:[0,0,1]
	v_med3_f32 v92, v92, s29, v227
	v_med3_f32 v93, v93, s29, v227
	v_med3_f32 v94, v94, s29, v227
	v_med3_f32 v95, v95, s29, v227
	v_cvt_pk_fp8_f32 v92, v92, v93
	v_cvt_pk_fp8_f32 v92, v94, v95 op_sel:[0,0,1]
	v_med3_f32 v84, v84, s29, v227
	v_med3_f32 v85, v85, s29, v227
	v_med3_f32 v86, v86, s29, v227
	v_med3_f32 v87, v87, s29, v227
	v_cvt_pk_fp8_f32 v93, v84, v85
	v_cvt_pk_fp8_f32 v93, v86, v87 op_sel:[0,0,1]
	v_med3_f32 v100, v100, s29, v227
	v_med3_f32 v101, v101, s29, v227
	v_med3_f32 v102, v102, s29, v227
	v_med3_f32 v103, v103, s29, v227
	v_cvt_pk_fp8_f32 v94, v100, v101
	v_cvt_pk_fp8_f32 v94, v102, v103 op_sel:[0,0,1]
	v_med3_f32 v96, v96, s29, v227
	v_med3_f32 v97, v97, s29, v227
	v_med3_f32 v98, v98, s29, v227
	v_med3_f32 v99, v99, s29, v227
	v_cvt_pk_fp8_f32 v95, v96, v97
	v_cvt_pk_fp8_f32 v95, v98, v99 op_sel:[0,0,1]
	v_med3_f32 v76, v76, s29, v227
	v_med3_f32 v77, v77, s29, v227
	v_med3_f32 v78, v78, s29, v227
	v_med3_f32 v79, v79, s29, v227
	v_cvt_pk_fp8_f32 v76, v76, v77
	v_cvt_pk_fp8_f32 v76, v78, v79 op_sel:[0,0,1]
	v_med3_f32 v72, v72, s29, v227
	v_med3_f32 v73, v73, s29, v227
	v_med3_f32 v74, v74, s29, v227
	v_med3_f32 v75, v75, s29, v227
	v_cvt_pk_fp8_f32 v77, v72, v73
	v_cvt_pk_fp8_f32 v77, v74, v75 op_sel:[0,0,1]
	v_med3_f32 v88, v88, s29, v227
	v_med3_f32 v89, v89, s29, v227
	v_med3_f32 v90, v90, s29, v227
	v_med3_f32 v91, v91, s29, v227
	v_cvt_pk_fp8_f32 v78, v88, v89
	v_cvt_pk_fp8_f32 v78, v90, v91 op_sel:[0,0,1]
	v_med3_f32 v68, v68, s29, v227
	v_med3_f32 v69, v69, s29, v227
	v_med3_f32 v70, v70, s29, v227
	v_med3_f32 v71, v71, s29, v227
	v_cvt_pk_fp8_f32 v79, v68, v69
	v_cvt_pk_fp8_f32 v79, v70, v71 op_sel:[0,0,1]
	s_barrier
	s_branch .LBB0_845
.Lg2q_w1_0:
	s_nop 15
	s_nop 3
	v_med3_f32 v128, v128, s29, v227
	v_med3_f32 v129, v129, s29, v227
	v_med3_f32 v130, v130, s29, v227
	v_med3_f32 v131, v131, s29, v227
	v_cvt_pk_fp8_f32 v128, v128, v129
	v_cvt_pk_fp8_f32 v128, v130, v131 op_sel:[0,0,1]
	v_med3_f32 v124, v124, s29, v227
	v_med3_f32 v125, v125, s29, v227
	v_med3_f32 v126, v126, s29, v227
	v_med3_f32 v127, v127, s29, v227
	v_cvt_pk_fp8_f32 v129, v124, v125
	v_cvt_pk_fp8_f32 v129, v126, v127 op_sel:[0,0,1]
	v_med3_f32 v160, v160, s29, v227
	v_med3_f32 v161, v161, s29, v227
	v_med3_f32 v162, v162, s29, v227
	v_med3_f32 v163, v163, s29, v227
	v_cvt_pk_fp8_f32 v130, v160, v161
	v_cvt_pk_fp8_f32 v130, v162, v163 op_sel:[0,0,1]
	v_med3_f32 v156, v156, s29, v227
	v_med3_f32 v157, v157, s29, v227
	v_med3_f32 v158, v158, s29, v227
	v_med3_f32 v159, v159, s29, v227
	v_cvt_pk_fp8_f32 v131, v156, v157
	v_cvt_pk_fp8_f32 v131, v158, v159 op_sel:[0,0,1]
	v_med3_f32 v108, v108, s29, v227
	v_med3_f32 v109, v109, s29, v227
	v_med3_f32 v110, v110, s29, v227
	v_med3_f32 v111, v111, s29, v227
	v_cvt_pk_fp8_f32 v108, v108, v109
	v_cvt_pk_fp8_f32 v108, v110, v111 op_sel:[0,0,1]
	v_med3_f32 v104, v104, s29, v227
	v_med3_f32 v105, v105, s29, v227
	v_med3_f32 v106, v106, s29, v227
	v_med3_f32 v107, v107, s29, v227
	v_cvt_pk_fp8_f32 v109, v104, v105
	v_cvt_pk_fp8_f32 v109, v106, v107 op_sel:[0,0,1]
	v_med3_f32 v140, v140, s29, v227
	v_med3_f32 v141, v141, s29, v227
	v_med3_f32 v142, v142, s29, v227
	v_med3_f32 v143, v143, s29, v227
	v_cvt_pk_fp8_f32 v110, v140, v141
	v_cvt_pk_fp8_f32 v110, v142, v143 op_sel:[0,0,1]
	v_med3_f32 v132, v132, s29, v227
	v_med3_f32 v133, v133, s29, v227
	v_med3_f32 v134, v134, s29, v227
	v_med3_f32 v135, v135, s29, v227
	v_cvt_pk_fp8_f32 v111, v132, v133
	v_cvt_pk_fp8_f32 v111, v134, v135 op_sel:[0,0,1]
	v_med3_f32 v92, v92, s29, v227
	v_med3_f32 v93, v93, s29, v227
	v_med3_f32 v94, v94, s29, v227
	v_med3_f32 v95, v95, s29, v227
	v_cvt_pk_fp8_f32 v92, v92, v93
	v_cvt_pk_fp8_f32 v92, v94, v95 op_sel:[0,0,1]
	v_med3_f32 v84, v84, s29, v227
	v_med3_f32 v85, v85, s29, v227
	v_med3_f32 v86, v86, s29, v227
	v_med3_f32 v87, v87, s29, v227
	v_cvt_pk_fp8_f32 v93, v84, v85
	v_cvt_pk_fp8_f32 v93, v86, v87 op_sel:[0,0,1]
	v_med3_f32 v100, v100, s29, v227
	v_med3_f32 v101, v101, s29, v227
	v_med3_f32 v102, v102, s29, v227
	v_med3_f32 v103, v103, s29, v227
	v_cvt_pk_fp8_f32 v94, v100, v101
	v_cvt_pk_fp8_f32 v94, v102, v103 op_sel:[0,0,1]
	v_med3_f32 v96, v96, s29, v227
	v_med3_f32 v97, v97, s29, v227
	v_med3_f32 v98, v98, s29, v227
	v_med3_f32 v99, v99, s29, v227
	v_cvt_pk_fp8_f32 v95, v96, v97
	v_cvt_pk_fp8_f32 v95, v98, v99 op_sel:[0,0,1]
	v_med3_f32 v76, v76, s29, v227
	v_med3_f32 v77, v77, s29, v227
	v_med3_f32 v78, v78, s29, v227
	v_med3_f32 v79, v79, s29, v227
	v_cvt_pk_fp8_f32 v76, v76, v77
	v_cvt_pk_fp8_f32 v76, v78, v79 op_sel:[0,0,1]
	v_med3_f32 v72, v72, s29, v227
	v_med3_f32 v73, v73, s29, v227
	v_med3_f32 v74, v74, s29, v227
	v_med3_f32 v75, v75, s29, v227
	v_cvt_pk_fp8_f32 v77, v72, v73
	v_cvt_pk_fp8_f32 v77, v74, v75 op_sel:[0,0,1]
	v_med3_f32 v88, v88, s29, v227
	v_med3_f32 v89, v89, s29, v227
	v_med3_f32 v90, v90, s29, v227
	v_med3_f32 v91, v91, s29, v227
	v_cvt_pk_fp8_f32 v78, v88, v89
	v_cvt_pk_fp8_f32 v78, v90, v91 op_sel:[0,0,1]
	v_med3_f32 v68, v68, s29, v227
	v_med3_f32 v69, v69, s29, v227
	v_med3_f32 v70, v70, s29, v227
	v_med3_f32 v71, v71, s29, v227
	v_cvt_pk_fp8_f32 v79, v68, v69
	v_cvt_pk_fp8_f32 v79, v70, v71 op_sel:[0,0,1]

; #define LAS __attribute__((address_space(3)))
;     __device__ __forceinline__ void operator()(const f32x4 (&acc)[2][2][4][2], const Unit& u, int wr, int wc, int fr, int fq) const {
;     ...
;         for (int sl = 0; sl < 4; ++sl) { const int ai = sl >> 1, mh = sl & 1;
;             asm volatile("s_waitcnt lgkmcnt(0)" ::: "memory"); __builtin_amdgcn_s_barrier();
;             const int rb = (sl & 1) ? B1 : B0, wb_ = (sl & 1) ? B0 : B1;
;             const u32x4 v0 = *(const LAS u32x4*)(lds + rb + rofs), v1 = *(const LAS u32x4*)(lds + rb + rofs4);
;             if (sl < 3) { const int a2 = (sl + 1) >> 1, m2 = ((sl + 1) & 1) * 2;
;                 const u32x4 wa = pack(acc, a2, m2), wb = pack(acc, a2, m2 + 1); *(LAS u32x4*)(lds + wb_ + wofs) = wa; *(LAS u32x4*)(lds + wb_ + wofs + 16 * 256) = wb; }
;             const int rl = ai * 128 + mh * 32 + t0;
;             if (!nost) { if (rl < u.nv) __builtin_nontemporal_store(v0, (u32x4*)(yp + (size_t)rl * D)); if (rl + 4 < u.nv) __builtin_nontemporal_store(v1, (u32x4*)(yp + (size_t)(rl + 4) * D)); } }
.LBB0_849:
	s_or_b64 exec, exec, s[4:5]
	s_waitcnt lgkmcnt(0)
	s_nop 0
	v_mov_b32_e32 v14, 0
	v_mov_b32_e32 v16, 0
	s_waitcnt lgkmcnt(0)
	s_barrier
	ds_read_b128 v[6:9], v248
	ds_read_b128 v[2:5], v249
	v_cmp_gt_i32_e32 vcc, s7, v214
	ds_write_b128 v207, v[128:131] offset:49152
	ds_write_b128 v207, v[108:111] offset:53248
	s_and_saveexec_b64 s[4:5], vcc
	s_cbranch_execz .LBB0_851
	v_lshl_add_u64 v[14:15], v[10:11], 0, v[216:217]
	s_waitcnt lgkmcnt(0)
	global_store_dwordx4 v[14:15], v[6:9], off nt

; #define LAS __attribute__((address_space(3)))
;     __device__ __forceinline__ void operator()(const f32x4 (&acc)[2][2][4][2], const Unit& u, int wr, int wc, int fr, int fq) const {
;     ...
;         for (int sl = 0; sl < 4; ++sl) { const int ai = sl >> 1, mh = sl & 1;
;             asm volatile("s_waitcnt lgkmcnt(0)" ::: "memory"); __builtin_amdgcn_s_barrier();
;             const int rb = (sl & 1) ? B1 : B0, wb_ = (sl & 1) ? B0 : B1;
;             const u32x4 v0 = *(const LAS u32x4*)(lds + rb + rofs), v1 = *(const LAS u32x4*)(lds + rb + rofs4);
;             if (sl < 3) { const int a2 = (sl + 1) >> 1, m2 = ((sl + 1) & 1) * 2;
;                 const u32x4 wa = pack(acc, a2, m2), wb = pack(acc, a2, m2 + 1); *(LAS u32x4*)(lds + wb_ + wofs) = wa; *(LAS u32x4*)(lds + wb_ + wofs + 16 * 256) = wb; }
;             const int rl = ai * 128 + mh * 32 + t0;
;             if (!nost) { if (rl < u.nv) __builtin_nontemporal_store(v0, (u32x4*)(yp + (size_t)rl * D)); if (rl + 4 < u.nv) __builtin_nontemporal_store(v1, (u32x4*)(yp + (size_t)(rl + 4) * D)); } }
.LBB0_853:
	s_or_b64 exec, exec, s[4:5]
	s_waitcnt lgkmcnt(0)
	s_nop 0
	v_mov_b32_e32 v14, 0
	v_mov_b32_e32 v16, 0
	s_waitcnt lgkmcnt(0)
	s_barrier
	ds_read_b128 v[6:9], v231 offset:49152
	ds_read_b128 v[2:5], v235 offset:49152
	v_cmp_gt_i32_e32 vcc, s7, v222
	ds_write_b128 v12, v[92:95]
	ds_write_b128 v211, v[76:79]
	s_and_saveexec_b64 s[4:5], vcc
	s_cbranch_execz .LBB0_855
	v_lshl_add_u64 v[12:13], v[10:11], 0, v[224:225]
	s_waitcnt lgkmcnt(0)
	global_store_dwordx4 v[12:13], v[6:9], off nt

; #define PG8_BAR __builtin_amdgcn_s_barrier()
;     ...
;         if constexpr (ALIGN_EPI) { if (wr == 0) PG8_BAR; }
;         if constexpr (Epi::F8) asm volatile("s_nop 15\n\ts_nop 15" ::: "memory");
;         if (!(probe & 2)) E(acc, cur, wr, wc, fr, fq);
;     __device__ __forceinline__ u32x4 pack(const f32x4 (&acc)[2][2][4][2], int ai, int m) const {
;         u32x4 w;
; #pragma unroll
;         for (int bj = 0; bj < 2; ++bj) {
;             f32x4 v0 = acc[ai][bj][m][0], v1 = acc[ai][bj][m][1];
; #pragma unroll
;             for (int j = 0; j < 4; ++j) { v0[j] = fminf(fmaxf(v0[j], -448.f), 448.f); v1[j] = fminf(fmaxf(v1[j], -448.f), 448.f); }
;             int w0 = __builtin_amdgcn_cvt_pk_fp8_f32(v0[0], v0[1], 0, false); w0 = __builtin_amdgcn_cvt_pk_fp8_f32(v0[2], v0[3], w0, true);
;             int w1 = __builtin_amdgcn_cvt_pk_fp8_f32(v1[0], v1[1], 0, false); w1 = __builtin_amdgcn_cvt_pk_fp8_f32(v1[2], v1[3], w1, true);
;             if (bj == 0) { w.x = (unsigned)w0; w.y = (unsigned)w1; } else { w.z = (unsigned)w0; w.w = (unsigned)w1; } }
;         return w;
;     }
.LBB0_1070:
	s_barrier
	s_andn2_b64 vcc, exec, s[52:53]
	s_cbranch_vccnz .Lg2q_w1_1
	s_nop 15
	s_nop 3
	v_med3_f32 v128, v128, s30, v227
	v_med3_f32 v129, v129, s30, v227
	v_med3_f32 v130, v130, s30, v227
	v_med3_f32 v131, v131, s30, v227
	v_cvt_pk_fp8_f32 v128, v128, v129
	v_cvt_pk_fp8_f32 v128, v130, v131 op_sel:[0,0,1]
	v_med3_f32 v124, v124, s30, v227
	v_med3_f32 v125, v125, s30, v227
	v_med3_f32 v126, v126, s30, v227
	v_med3_f32 v127, v127, s30, v227
	v_cvt_pk_fp8_f32 v129, v124, v125
	v_cvt_pk_fp8_f32 v129, v126, v127 op_sel:[0,0,1]
	v_med3_f32 v160, v160, s30, v227
	v_med3_f32 v161, v161, s30, v227
	v_med3_f32 v162, v162, s30, v227
	v_med3_f32 v163, v163, s30, v227
	v_cvt_pk_fp8_f32 v130, v160, v161
	v_cvt_pk_fp8_f32 v130, v162, v163 op_sel:[0,0,1]
	v_med3_f32 v156, v156, s30, v227
	v_med3_f32 v157, v157, s30, v227
	v_med3_f32 v158, v158, s30, v227
	v_med3_f32 v159, v159, s30, v227
	v_cvt_pk_fp8_f32 v131, v156, v157
	v_cvt_pk_fp8_f32 v131, v158, v159 op_sel:[0,0,1]
	v_med3_f32 v108, v108, s30, v227
	v_med3_f32 v109, v109, s30, v227
	v_med3_f32 v110, v110, s30, v227
	v_med3_f32 v111, v111, s30, v227
	v_cvt_pk_fp8_f32 v108, v108, v109
	v_cvt_pk_fp8_f32 v108, v110, v111 op_sel:[0,0,1]
	v_med3_f32 v104, v104, s30, v227
	v_med3_f32 v105, v105, s30, v227
	v_med3_f32 v106, v106, s30, v227
	v_med3_f32 v107, v107, s30, v227
	v_cvt_pk_fp8_f32 v109, v104, v105
	v_cvt_pk_fp8_f32 v109, v106, v107 op_sel:[0,0,1]
	v_med3_f32 v140, v140, s30, v227
	v_med3_f32 v141, v141, s30, v227
	v_med3_f32 v142, v142, s30, v227
	v_med3_f32 v143, v143, s30, v227
	v_cvt_pk_fp8_f32 v110, v140, v141
	v_cvt_pk_fp8_f32 v110, v142, v143 op_sel:[0,0,1]
	v_med3_f32 v132, v132, s30, v227
	v_med3_f32 v133, v133, s30, v227
	v_med3_f32 v134, v134, s30, v227
	v_med3_f32 v135, v135, s30, v227
	v_cvt_pk_fp8_f32 v111, v132, v133
	v_cvt_pk_fp8_f32 v111, v134, v135 op_sel:[0,0,1]
	v_med3_f32 v92, v92, s30, v227
	v_med3_f32 v93, v93, s30, v227
	v_med3_f32 v94, v94, s30, v227
	v_med3_f32 v95, v95, s30, v227
	v_cvt_pk_fp8_f32 v92, v92, v93
	v_cvt_pk_fp8_f32 v92, v94, v95 op_sel:[0,0,1]
	v_med3_f32 v84, v84, s30, v227
	v_med3_f32 v85, v85, s30, v227
	v_med3_f32 v86, v86, s30, v227
	v_med3_f32 v87, v87, s30, v227
	v_cvt_pk_fp8_f32 v93, v84, v85
	v_cvt_pk_fp8_f32 v93, v86, v87 op_sel:[0,0,1]
	v_med3_f32 v100, v100, s30, v227
	v_med3_f32 v101, v101, s30, v227
	v_med3_f32 v102, v102, s30, v227
	v_med3_f32 v103, v103, s30, v227
	v_cvt_pk_fp8_f32 v94, v100, v101
	v_cvt_pk_fp8_f32 v94, v102, v103 op_sel:[0,0,1]
	v_med3_f32 v96, v96, s30, v227
	v_med3_f32 v97, v97, s30, v227
	v_med3_f32 v98, v98, s30, v227
	v_med3_f32 v99, v99, s30, v227
	v_cvt_pk_fp8_f32 v95, v96, v97
	v_cvt_pk_fp8_f32 v95, v98, v99 op_sel:[0,0,1]
	v_med3_f32 v76, v76, s30, v227
	v_med3_f32 v77, v77, s30, v227
	v_med3_f32 v78, v78, s30, v227
	v_med3_f32 v79, v79, s30, v227
	v_cvt_pk_fp8_f32 v76, v76, v77
	v_cvt_pk_fp8_f32 v76, v78, v79 op_sel:[0,0,1]
	v_med3_f32 v72, v72, s30, v227
	v_med3_f32 v73, v73, s30, v227
	v_med3_f32 v74, v74, s30, v227
	v_med3_f32 v75, v75, s30, v227
	v_cvt_pk_fp8_f32 v77, v72, v73
	v_cvt_pk_fp8_f32 v77, v74, v75 op_sel:[0,0,1]
	v_med3_f32 v88, v88, s30, v227
	v_med3_f32 v89, v89, s30, v227
	v_med3_f32 v90, v90, s30, v227
	v_med3_f32 v91, v91, s30, v227
	v_cvt_pk_fp8_f32 v78, v88, v89
	v_cvt_pk_fp8_f32 v78, v90, v91 op_sel:[0,0,1]
	v_med3_f32 v68, v68, s30, v227
	v_med3_f32 v69, v69, s30, v227
	v_med3_f32 v70, v70, s30, v227
	v_med3_f32 v71, v71, s30, v227
	v_cvt_pk_fp8_f32 v79, v68, v69
	v_cvt_pk_fp8_f32 v79, v70, v71 op_sel:[0,0,1]
	s_barrier
	s_branch .LBB0_1072
.Lg2q_w1_1:
	s_nop 15
	s_nop 3
	v_med3_f32 v128, v128, s30, v227
	v_med3_f32 v129, v129, s30, v227
	v_med3_f32 v130, v130, s30, v227
	v_med3_f32 v131, v131, s30, v227
	v_cvt_pk_fp8_f32 v128, v128, v129
	v_cvt_pk_fp8_f32 v128, v130, v131 op_sel:[0,0,1]
	v_med3_f32 v124, v124, s30, v227
	v_med3_f32 v125, v125, s30, v227
	v_med3_f32 v126, v126, s30, v227
	v_med3_f32 v127, v127, s30, v227
	v_cvt_pk_fp8_f32 v129, v124, v125
	v_cvt_pk_fp8_f32 v129, v126, v127 op_sel:[0,0,1]
	v_med3_f32 v160, v160, s30, v227
	v_med3_f32 v161, v161, s30, v227
	v_med3_f32 v162, v162, s30, v227
	v_med3_f32 v163, v163, s30, v227
	v_cvt_pk_fp8_f32 v130, v160, v161
	v_cvt_pk_fp8_f32 v130, v162, v163 op_sel:[0,0,1]
	v_med3_f32 v156, v156, s30, v227
	v_med3_f32 v157, v157, s30, v227
	v_med3_f32 v158, v158, s30, v227
	v_med3_f32 v159, v159, s30, v227
	v_cvt_pk_fp8_f32 v131, v156, v157
	v_cvt_pk_fp8_f32 v131, v158, v159 op_sel:[0,0,1]
	v_med3_f32 v108, v108, s30, v227
	v_med3_f32 v109, v109, s30, v227
	v_med3_f32 v110, v110, s30, v227
	v_med3_f32 v111, v111, s30, v227
	v_cvt_pk_fp8_f32 v108, v108, v109
	v_cvt_pk_fp8_f32 v108, v110, v111 op_sel:[0,0,1]
	v_med3_f32 v104, v104, s30, v227
	v_med3_f32 v105, v105, s30, v227
	v_med3_f32 v106, v106, s30, v227
	v_med3_f32 v107, v107, s30, v227
	v_cvt_pk_fp8_f32 v109, v104, v105
	v_cvt_pk_fp8_f32 v109, v106, v107 op_sel:[0,0,1]
	v_med3_f32 v140, v140, s30, v227
	v_med3_f32 v141, v141, s30, v227
	v_med3_f32 v142, v142, s30, v227
	v_med3_f32 v143, v143, s30, v227
	v_cvt_pk_fp8_f32 v110, v140, v141
	v_cvt_pk_fp8_f32 v110, v142, v143 op_sel:[0,0,1]
	v_med3_f32 v132, v132, s30, v227
	v_med3_f32 v133, v133, s30, v227
	v_med3_f32 v134, v134, s30, v227
	v_med3_f32 v135, v135, s30, v227
	v_cvt_pk_fp8_f32 v111, v132, v133
	v_cvt_pk_fp8_f32 v111, v134, v135 op_sel:[0,0,1]
	v_med3_f32 v92, v92, s30, v227
	v_med3_f32 v93, v93, s30, v227
	v_med3_f32 v94, v94, s30, v227
	v_med3_f32 v95, v95, s30, v227
	v_cvt_pk_fp8_f32 v92, v92, v93
	v_cvt_pk_fp8_f32 v92, v94, v95 op_sel:[0,0,1]
	v_med3_f32 v84, v84, s30, v227
	v_med3_f32 v85, v85, s30, v227
	v_med3_f32 v86, v86, s30, v227
	v_med3_f32 v87, v87, s30, v227
	v_cvt_pk_fp8_f32 v93, v84, v85
	v_cvt_pk_fp8_f32 v93, v86, v87 op_sel:[0,0,1]
	v_med3_f32 v100, v100, s30, v227
	v_med3_f32 v101, v101, s30, v227
	v_med3_f32 v102, v102, s30, v227
	v_med3_f32 v103, v103, s30, v227
	v_cvt_pk_fp8_f32 v94, v100, v101
	v_cvt_pk_fp8_f32 v94, v102, v103 op_sel:[0,0,1]
	v_med3_f32 v96, v96, s30, v227
	v_med3_f32 v97, v97, s30, v227
	v_med3_f32 v98, v98, s30, v227
	v_med3_f32 v99, v99, s30, v227
	v_cvt_pk_fp8_f32 v95, v96, v97
	v_cvt_pk_fp8_f32 v95, v98, v99 op_sel:[0,0,1]
	v_med3_f32 v76, v76, s30, v227
	v_med3_f32 v77, v77, s30, v227
	v_med3_f32 v78, v78, s30, v227
	v_med3_f32 v79, v79, s30, v227
	v_cvt_pk_fp8_f32 v76, v76, v77
	v_cvt_pk_fp8_f32 v76, v78, v79 op_sel:[0,0,1]
	v_med3_f32 v72, v72, s30, v227
	v_med3_f32 v73, v73, s30, v227
	v_med3_f32 v74, v74, s30, v227
	v_med3_f32 v75, v75, s30, v227
	v_cvt_pk_fp8_f32 v77, v72, v73
	v_cvt_pk_fp8_f32 v77, v74, v75 op_sel:[0,0,1]
	v_med3_f32 v88, v88, s30, v227
	v_med3_f32 v89, v89, s30, v227
	v_med3_f32 v90, v90, s30, v227
	v_med3_f32 v91, v91, s30, v227
	v_cvt_pk_fp8_f32 v78, v88, v89
	v_cvt_pk_fp8_f32 v78, v90, v91 op_sel:[0,0,1]
	v_med3_f32 v68, v68, s30, v227
	v_med3_f32 v69, v69, s30, v227
	v_med3_f32 v70, v70, s30, v227
	v_med3_f32 v71, v71, s30, v227
	v_cvt_pk_fp8_f32 v79, v68, v69
	v_cvt_pk_fp8_f32 v79, v70, v71 op_sel:[0,0,1]

; #define LAS __attribute__((address_space(3)))
;     __device__ __forceinline__ void operator()(const f32x4 (&acc)[2][2][4][2], const Unit& u, int wr, int wc, int fr, int fq) const {
;     ...
;         for (int sl = 0; sl < 4; ++sl) { const int ai = sl >> 1, mh = sl & 1;
;             asm volatile("s_waitcnt lgkmcnt(0)" ::: "memory"); __builtin_amdgcn_s_barrier();
;             const int rb = (sl & 1) ? B1 : B0, wb_ = (sl & 1) ? B0 : B1;
;             const u32x4 v0 = *(const LAS u32x4*)(lds + rb + rofs), v1 = *(const LAS u32x4*)(lds + rb + rofs4);
;             if (sl < 3) { const int a2 = (sl + 1) >> 1, m2 = ((sl + 1) & 1) * 2;
;                 const u32x4 wa = pack(acc, a2, m2), wb = pack(acc, a2, m2 + 1); *(LAS u32x4*)(lds + wb_ + wofs) = wa; *(LAS u32x4*)(lds + wb_ + wofs + 16 * 256) = wb; }
;             const int rl = ai * 128 + mh * 32 + t0;
;             if (!nost) { if (rl < u.nv) __builtin_nontemporal_store(v0, (u32x4*)(yp + (size_t)rl * D)); if (rl + 4 < u.nv) __builtin_nontemporal_store(v1, (u32x4*)(yp + (size_t)(rl + 4) * D)); } }
.LBB0_1076:
	s_or_b64 exec, exec, s[4:5]
	s_waitcnt lgkmcnt(0)
	s_nop 0
	v_mov_b32_e32 v14, 0
	v_mov_b32_e32 v16, 0
	s_waitcnt lgkmcnt(0)
	s_barrier
	ds_read_b128 v[6:9], v248
	ds_read_b128 v[2:5], v249
	v_cmp_gt_i32_e32 vcc, s6, v214
	ds_write_b128 v207, v[128:131] offset:49152
	ds_write_b128 v207, v[108:111] offset:53248
	s_and_saveexec_b64 s[4:5], vcc
	s_cbranch_execz .LBB0_1078
	v_lshl_add_u64 v[14:15], v[10:11], 0, v[216:217]
	s_waitcnt lgkmcnt(0)
	global_store_dwordx4 v[14:15], v[6:9], off nt

; #define LAS __attribute__((address_space(3)))
;     __device__ __forceinline__ void operator()(const f32x4 (&acc)[2][2][4][2], const Unit& u, int wr, int wc, int fr, int fq) const {
;     ...
;         for (int sl = 0; sl < 4; ++sl) { const int ai = sl >> 1, mh = sl & 1;
;             asm volatile("s_waitcnt lgkmcnt(0)" ::: "memory"); __builtin_amdgcn_s_barrier();
;             const int rb = (sl & 1) ? B1 : B0, wb_ = (sl & 1) ? B0 : B1;
;             const u32x4 v0 = *(const LAS u32x4*)(lds + rb + rofs), v1 = *(const LAS u32x4*)(lds + rb + rofs4);
;             if (sl < 3) { const int a2 = (sl + 1) >> 1, m2 = ((sl + 1) & 1) * 2;
;                 const u32x4 wa = pack(acc, a2, m2), wb = pack(acc, a2, m2 + 1); *(LAS u32x4*)(lds + wb_ + wofs) = wa; *(LAS u32x4*)(lds + wb_ + wofs + 16 * 256) = wb; }
;             const int rl = ai * 128 + mh * 32 + t0;
;             if (!nost) { if (rl < u.nv) __builtin_nontemporal_store(v0, (u32x4*)(yp + (size_t)rl * D)); if (rl + 4 < u.nv) __builtin_nontemporal_store(v1, (u32x4*)(yp + (size_t)(rl + 4) * D)); } }
.LBB0_1080:
	s_or_b64 exec, exec, s[4:5]
	s_waitcnt lgkmcnt(0)
	s_nop 0
	v_mov_b32_e32 v14, 0
	v_mov_b32_e32 v16, 0
	s_waitcnt lgkmcnt(0)
	s_barrier
	ds_read_b128 v[6:9], v231 offset:49152
	ds_read_b128 v[2:5], v235 offset:49152
	v_cmp_gt_i32_e32 vcc, s6, v222
	ds_write_b128 v12, v[92:95]
	ds_write_b128 v211, v[76:79]
	s_and_saveexec_b64 s[4:5], vcc
	s_cbranch_execz .LBB0_1082
	v_lshl_add_u64 v[12:13], v[10:11], 0, v[224:225]
	s_waitcnt lgkmcnt(0)
	global_store_dwordx4 v[12:13], v[6:9], off nt
